# RWKV scan: static s_setprio 2 for the recurrence waves (restored at phase end)
# baseline (speedup 1.0000x reference)
; #define LAS __attribute__((address_space(3)))
; template <class AT_>
; __device__ __forceinline__ void rwkv_scan_phase(const AT_& a, Frame& F, int j) {
;     ...
;             if (w < 4) {
;                 if (blk >= 0 && blk < RW_NBLK) {
;                     const LAS float* ob = (const LAS float*)(F.lds + (blk & 1) * OPB); LAS float* Yb = Ybase + (blk & 1) * (RW_T * 64);
;                     auto ld = [&](int t) { RwOps o; const LAS float* p = ob + t * 64 + 8 * kg;
;                         o.a0 = *(const LAS f32x4*)p; o.a1 = *(const LAS f32x4*)(p + 4); p += RW_T * 64; o.r0 = *(const LAS f32x4*)p; o.r1 = *(const LAS f32x4*)(p + 4); p += RW_T * 64;
;                         o.w0 = *(const LAS f32x4*)p; o.w1 = *(const LAS f32x4*)(p + 4); p += RW_T * 64; o.b0 = *(const LAS f32x4*)p; o.b1 = *(const LAS f32x4*)(p + 4); p += RW_T * 64;
;                         o.k0 = *(const LAS f32x4*)p; o.k1 = *(const LAS f32x4*)(p + 4);
;                         o.v = *(const LAS f32x2*)(ob + 5 * RW_T * 64 + t * 64 + v0); o.sc = *(const LAS f32x2*)(ob + 6 * RW_T * 64 + t * 4); return o; };
;     ...
;                     RwOps oa = ld(0);
.LBB0_3512:
	s_and_b64 vcc, exec, s[42:43]
	s_cbranch_vccz .LBB0_3487
	s_cmp_lt_i32 s90, 0
	s_cselect_b64 s[42:43], -1, 0
	s_cmpk_eq_i32 s90, 0x80
	s_cselect_b64 s[44:45], -1, 0
	s_or_b64 s[42:43], s[42:43], s[44:45]
	s_and_b64 vcc, exec, s[42:43]
	s_cbranch_vccnz .LBB0_3487
	s_setprio 2
	s_and_b32 s98, s90, 1
	s_mul_i32 s99, s98, 0xc200
	s_add_i32 s99, s99, s53
	v_add_u32_e32 v50, s99, v166
	v_add_u32_e32 v51, s99, v167
	v_add_u32_e32 v51, 40960, v51
	v_mov_b32_e32 v52, s99
	v_add_u32_e32 v52, 49152, v52
	s_lshl_b32 s98, s98, 13
	s_add_i32 s98, s98, s53
	s_add_i32 s98, s98, 0x18400
	v_add_u32_e32 v53, s98, v167
	ds_read_b128 v[168:171], v50 offset:0
	ds_read_b128 v[172:175], v50 offset:16
	ds_read_b128 v[176:179], v50 offset:8192
	ds_read_b128 v[180:183], v50 offset:8208
	ds_read_b128 v[184:187], v50 offset:16384
	ds_read_b128 v[188:191], v50 offset:16400
	ds_read_b128 v[192:195], v50 offset:24576
	ds_read_b128 v[196:199], v50 offset:24592
	ds_read_b128 v[200:203], v50 offset:32768
	ds_read_b128 v[204:207], v50 offset:32784
	ds_read2_b64 v[212:215], v51 offset0:0 offset1:32
	ds_read2_b64 v[216:219], v52 offset0:0 offset1:2
	v_add_u32_e32 v51, 512, v51
	v_add_u32_e32 v52, 32, v52
	s_mov_b32 s98, 4

; __device__ __forceinline__ unsigned xb_ld(unsigned* p)              { return __hip_atomic_load(p, __ATOMIC_RELAXED, __HIP_MEMORY_SCOPE_AGENT); }
; __device__ __forceinline__ void xcd_barrier_complete(unsigned* bar, unsigned x, unsigned& nloc, unsigned& nx) {
;     const unsigned G = gridDim.x * gridDim.y * gridDim.z;
;     unsigned sum, cnt, mine, sp = 0u;
;     for (;;) {
;         sum = 0u; cnt = 0u; mine = 0u;
; #pragma unroll
;         for (unsigned j = 0; j < 16; ++j) { const unsigned c = xb_ld(&bar[XB_XCNT(j)]); sum += c; cnt += (c > 0u) ? 1u : 0u; mine = (j == x) ? c : mine; }
;         if (sum == G) break;
;         __builtin_amdgcn_s_sleep(1);
;         if ((++sp & 255u) == 0u) { if (xb_ld(&bar[XB_TMO])) break; if (sp > XB_SPIN_CAP) { atomicAdd(&bar[XB_TMO], 1u); break; } }
;     }
;     nloc = mine > 0u ? mine : 1u; nx = cnt > 0u ? cnt : 1u;
; }
; __device__ __forceinline__ void xcd_barrier(const XcdBarrier& b) {
;     asm volatile("s_waitcnt vmcnt(0)" ::: "memory");
;     __syncthreads();
;     if (threadIdx.x == 0) {
;         unsigned* bar = b.bar;
;         __builtin_amdgcn_s_waitcnt(0);
;         unsigned nloc = b.st[0], nx = b.st[1];
;         if (nloc == 0u) { xcd_barrier_complete(bar, b.x, nloc, nx); b.st[0] = nloc; b.st[1] = nx; }
.LBB0_3521:
	s_setprio 0
	v_readlane_b32 s7, v247, 8
	s_cmp_lt_i32 s7, 35
	v_readlane_b32 s76, v247, 9
	s_cbranch_scc1 .LBB0_3567
	v_readlane_b32 s34, v247, 2
	v_readlane_b32 s35, v247, 3
	s_waitcnt vmcnt(0)
	s_barrier
	s_mov_b64 s[30:31], exec
	v_readlane_b32 s0, v247, 5
	v_readlane_b32 s1, v247, 6
	s_and_b64 s[0:1], s[30:31], s[0:1]
	s_mov_b64 exec, s[0:1]
	s_cbranch_execz .LBB0_3566
	s_add_i32 s0, 0, 0x20160
	v_mov_b32_e32 v1, s0
	s_waitcnt vmcnt(0) expcnt(0) lgkmcnt(0)
	ds_read_b32 v4, v1
	s_add_i32 s0, 0, 0x20164
	v_mov_b32_e32 v1, s0
	ds_read_b32 v2, v1
	s_waitcnt lgkmcnt(1)
	v_cmp_ne_u32_e32 vcc, 0, v4
	s_cbranch_vccnz .LBB0_3537
	s_add_u32 s2, s34, 0x1000
	s_addc_u32 s3, s35, 0
	s_load_dwordx2 s[0:1], s[12:13], 0x4
	s_add_u32 s4, s34, 0x1100
	s_addc_u32 s5, s35, 0
	s_add_u32 s6, s34, 0x1200
	s_addc_u32 s7, s35, 0
	s_add_u32 s8, s34, 0x1300
	s_waitcnt lgkmcnt(0)
	s_mul_i32 s18, s0, s33
	s_addc_u32 s9, s35, 0
	s_mul_i32 s18, s18, s1
	s_mov_b32 s19, 1
	s_mov_b64 s[0:1], 0
	v_mov_b64_e32 v[2:3], s[34:35]
	v_mov_b64_e32 v[4:5], s[2:3]
	v_mov_b64_e32 v[6:7], s[4:5]
	v_mov_b64_e32 v[8:9], s[6:7]
	v_mov_b64_e32 v[10:11], s[8:9]
	s_branch .LBB0_3527
